# v24 + dilated-attention mixing loop software-pipelined by one trip (next trip's loads issued before the current trip's arithmetic)
# baseline (speedup 1.0000x reference)
.LBB0_341:
	s_lshl_b32 s3, s74, 10
	s_or_b32 s20, s20, s3
	s_waitcnt vmcnt(0)
	s_barrier
	s_waitcnt vmcnt(0)
	buffer_inv sc1
	s_waitcnt vmcnt(0)
	v_and_b32_e32 v2, 56, v180
	s_add_u32 s4, s46, s77
	s_addc_u32 s5, s47, 0
	v_lshlrev_b32_e32 v168, 1, v2
	v_lshl_add_u64 v[0:1], s[4:5], 0, v[168:169]
	s_mov_b32 s3, 0
	v_lshlrev_b32_e32 v168, 1, v2
	s_nop 0
	v_add_u32_e32 v242, s3, v179
	v_ashrrev_i32_e32 v242, 3, v242
	v_ashrrev_i32_e32 v243, 31, v242
	v_lshl_add_u64 v[244:245], v[242:243], 2, s[14:15]
	v_add_co_u32_e32 v248, vcc, 0x1000, v244
	v_lshlrev_b64 v[246:247], 7, v[242:243]
	s_nop 0
	v_addc_co_u32_e32 v249, vcc, 0, v245, vcc
	v_lshl_add_u64 v[242:243], s[20:21], 0, v[242:243]
	global_load_dword v224, v[244:245], off
	v_lshl_add_u64 v[246:247], s[12:13], 0, v[246:247]
	v_add_co_u32_e32 v244, vcc, 0x2000, v244
	s_mov_b32 s4, 0x20000
	v_lshlrev_b64 v[242:243], 11, v[242:243]
	v_lshl_add_u64 v[246:247], v[246:247], 0, v[168:169]
	v_addc_co_u32_e32 v245, vcc, 0, v245, vcc
	v_lshl_add_u64 v[240:241], v[0:1], 0, v[242:243]
	v_add_co_u32_e32 v242, vcc, s4, v246
	s_mov_b32 s5, 0x40000
	s_nop 0
	v_addc_co_u32_e32 v243, vcc, 0, v247, vcc
	v_add_co_u32_e32 v250, vcc, s5, v246
	s_addk_i32 s3, 0x200
	s_nop 0
	v_addc_co_u32_e32 v251, vcc, 0, v247, vcc
	global_load_dword v225, v[248:249], off
	global_load_dword v226, v[244:245], off
	s_nop 0
	global_load_dwordx4 v[228:231], v[242:243], off
	s_nop 0
	global_load_dwordx4 v[232:235], v[246:247], off
	s_nop 0
	global_load_dwordx4 v[236:239], v[250:251], off
	s_waitcnt vmcnt(0)
	s_branch .Lmix_body
.LBB0_342:
	s_waitcnt vmcnt(1)
.Lmix_body:
	v_mov_b32_e32 v30, v224
	v_mov_b32_e32 v31, v225
	v_mov_b32_e32 v32, v226
	v_mov_b32_e32 v2, v228
	v_mov_b32_e32 v3, v229
	v_mov_b32_e32 v4, v230
	v_mov_b32_e32 v5, v231
	v_mov_b32_e32 v6, v232
	v_mov_b32_e32 v7, v233
	v_mov_b32_e32 v8, v234
	v_mov_b32_e32 v9, v235
	v_mov_b32_e32 v10, v236
	v_mov_b32_e32 v11, v237
	v_mov_b32_e32 v12, v238
	v_mov_b32_e32 v13, v239
	v_mov_b32_e32 v14, v240
	v_mov_b32_e32 v15, v241
	s_cmpk_eq_i32 s3, 0x2000
	s_cbranch_scc1 .Lmix_nopf
	s_nop 0
	v_add_u32_e32 v242, s3, v179
	v_ashrrev_i32_e32 v242, 3, v242
	v_ashrrev_i32_e32 v243, 31, v242
	v_lshl_add_u64 v[244:245], v[242:243], 2, s[14:15]
	v_add_co_u32_e32 v248, vcc, 0x1000, v244
	v_lshlrev_b64 v[246:247], 7, v[242:243]
	s_nop 0
	v_addc_co_u32_e32 v249, vcc, 0, v245, vcc
	v_lshl_add_u64 v[242:243], s[20:21], 0, v[242:243]
	global_load_dword v224, v[244:245], off
	v_lshl_add_u64 v[246:247], s[12:13], 0, v[246:247]
	v_add_co_u32_e32 v244, vcc, 0x2000, v244
	s_mov_b32 s4, 0x20000
	v_lshlrev_b64 v[242:243], 11, v[242:243]
	v_lshl_add_u64 v[246:247], v[246:247], 0, v[168:169]
	v_addc_co_u32_e32 v245, vcc, 0, v245, vcc
	v_lshl_add_u64 v[240:241], v[0:1], 0, v[242:243]
	v_add_co_u32_e32 v242, vcc, s4, v246
	s_mov_b32 s5, 0x40000
	s_nop 0
	v_addc_co_u32_e32 v243, vcc, 0, v247, vcc
	v_add_co_u32_e32 v250, vcc, s5, v246
	s_addk_i32 s3, 0x200
	s_nop 0
	v_addc_co_u32_e32 v251, vcc, 0, v247, vcc
	global_load_dword v225, v[248:249], off
	global_load_dword v226, v[244:245], off
	s_nop 0
	global_load_dwordx4 v[228:231], v[242:243], off
	s_nop 0
	global_load_dwordx4 v[232:235], v[246:247], off
	s_nop 0
	global_load_dwordx4 v[236:239], v[250:251], off
	s_branch .Lmix_comp
.Lmix_nopf:
	s_addk_i32 s3, 0x200
.Lmix_comp:
	v_max3_f32 v33, v30, v31, v32
	v_lshlrev_b32_e32 v16, 16, v2
	v_lshlrev_b32_e32 v18, 16, v6
	v_lshlrev_b32_e32 v20, 16, v10
	v_and_b32_e32 v22, 0xffff0000, v2
	v_and_b32_e32 v2, 0xffff0000, v6
	v_and_b32_e32 v6, 0xffff0000, v10
	v_lshlrev_b32_e32 v10, 16, v4
	v_lshlrev_b32_e32 v24, 16, v8
	v_lshlrev_b32_e32 v26, 16, v12
	v_and_b32_e32 v28, 0xffff0000, v4
	v_and_b32_e32 v4, 0xffff0000, v8
	v_and_b32_e32 v8, 0xffff0000, v12
	v_sub_f32_e32 v12, v30, v33
	v_sub_f32_e32 v30, v31, v33
	v_lshlrev_b32_e32 v17, 16, v7
	v_lshlrev_b32_e32 v21, 16, v11
	v_and_b32_e32 v23, 0xffff0000, v7
	v_and_b32_e32 v7, 0xffff0000, v11
	v_lshlrev_b32_e32 v11, 16, v9
	v_lshlrev_b32_e32 v27, 16, v13
	v_and_b32_e32 v29, 0xffff0000, v9
	v_and_b32_e32 v9, 0xffff0000, v13
	v_sub_f32_e32 v31, v32, v33
	v_exp_f32_e32 v13, v12
	v_exp_f32_e32 v12, v30
	v_exp_f32_e32 v31, v31
	v_lshlrev_b32_e32 v19, 16, v3
	v_and_b32_e32 v3, 0xffff0000, v3
	v_add_f32_e32 v30, v13, v12
	v_add_f32_e32 v30, v31, v30
	v_div_scale_f32 v32, s[4:5], v30, v30, 1.0
	v_rcp_f32_e32 v34, v32
	v_div_scale_f32 v33, vcc, 1.0, v30, 1.0
	v_lshlrev_b32_e32 v25, 16, v5
	v_fma_f32 v35, -v32, v34, 1.0
	v_fmac_f32_e32 v34, v35, v34
	v_mul_f32_e32 v35, v33, v34
	v_fma_f32 v36, -v32, v35, v33
	v_fmac_f32_e32 v35, v36, v34
	v_fma_f32 v32, -v32, v35, v33
	v_div_fmas_f32 v32, v32, v34, v35
	v_div_fixup_f32 v30, v32, v30, 1.0
	v_and_b32_e32 v5, 0xffff0000, v5
	v_pk_mul_f32 v[12:13], v[12:13], v[30:31] op_sel_hi:[1,0]
	v_mul_f32_e32 v32, v31, v30
	v_pk_mul_f32 v[18:19], v[12:13], v[18:19] op_sel:[1,0] op_sel_hi:[0,1]
	v_pk_mul_f32 v[2:3], v[12:13], v[2:3] op_sel:[1,0] op_sel_hi:[0,1]
	v_pk_mul_f32 v[24:25], v[12:13], v[24:25] op_sel:[1,0] op_sel_hi:[0,1]
	v_pk_mul_f32 v[4:5], v[12:13], v[4:5] op_sel:[1,0] op_sel_hi:[0,1]
	v_pk_fma_f32 v[16:17], v[12:13], v[16:17], v[18:19]
	v_pk_fma_f32 v[2:3], v[12:13], v[22:23], v[2:3]
	v_pk_fma_f32 v[10:11], v[12:13], v[10:11], v[24:25]
	v_pk_fma_f32 v[4:5], v[12:13], v[28:29], v[4:5]
	v_pk_fma_f32 v[12:13], v[32:33], v[20:21], v[16:17] op_sel_hi:[0,1,1]
	v_pk_fma_f32 v[2:3], v[32:33], v[6:7], v[2:3] op_sel_hi:[0,1,1]
	v_pk_fma_f32 v[6:7], v[32:33], v[26:27], v[10:11] op_sel_hi:[0,1,1]
	v_pk_fma_f32 v[4:5], v[32:33], v[8:9], v[4:5] op_sel_hi:[0,1,1]
	v_bfe_u32 v8, v5, 16, 1
	v_bfe_u32 v9, v4, 16, 1
	v_bfe_u32 v16, v12, 16, 1
	v_bfe_u32 v17, v13, 16, 1
	v_bfe_u32 v18, v6, 16, 1
	v_bfe_u32 v19, v7, 16, 1
	v_bfe_u32 v10, v3, 16, 1
	v_bfe_u32 v11, v2, 16, 1
	v_add3_u32 v4, v4, v9, s70
	v_add3_u32 v5, v5, v8, s70
	v_add3_u32 v7, v7, v19, s70
	v_add3_u32 v6, v6, v18, s70
	v_add3_u32 v8, v13, v17, s70
	v_add3_u32 v9, v12, v16, s70
	v_add3_u32 v2, v2, v11, s70
	v_add3_u32 v3, v3, v10, s70
	v_lshrrev_b32_e32 v9, 16, v9
	v_lshrrev_b32_e32 v8, 16, v8
	v_lshrrev_b32_e32 v6, 16, v6
	v_lshrrev_b32_e32 v7, 16, v7
	v_and_or_b32 v5, v5, s61, v7
	v_and_or_b32 v4, v4, s61, v6
	v_and_or_b32 v3, v3, s61, v8
	v_and_or_b32 v2, v2, s61, v9
	global_store_dwordx4 v[14:15], v[2:5], off offset:1024
	s_cmpk_lg_i32 s3, 0x2200
	s_cbranch_scc1 .LBB0_342
	s_waitcnt vmcnt(0)
	s_add_i32 s71, s71, s33
	s_cmpk_lt_i32 s71, 0x200
	s_barrier
	s_cbranch_scc1 .LBB0_278
	v_readlane_b32 s6, v255, 9
	v_readlane_b32 s7, v255, 10
